# v16 + 400 (instead of 208) w_down strips per layer converted by work items at the end of the mixer queues rather than in the prologue
# speedup vs baseline: 1.0038x; 1.0038x over previous
.LBB0_50:
	s_or_b64 exec, exec, s[10:11]
	v_readlane_b32 s0, v251, 2
	s_cmpk_eq_i32 s0, 0x100
	s_cselect_b64 s[10:11], -1, 0
	s_and_b64 s[0:1], s[10:11], exec
	s_cselect_b32 s36, 15, 0
	s_movk_i32 s0, 0x63a
	s_cselect_b32 s0, s0, 0x98c
	s_and_b32 s1, s36, 1
	s_bitcmp1_b32 s36, 0
	s_cselect_b64 s[4:5], -1, 0
	s_cmp_eq_u32 s1, 0
	s_movk_i32 s1, 0x1c9
	s_cselect_b32 s1, s1, 0x84
	s_not_b32 s6, s36
	s_lshl_b32 s6, s6, 7
	s_and_b32 s8, s6, 0x100
	s_and_b32 s9, s36, 4
	s_bitcmp1_b32 s36, 2
	s_cselect_b64 s[6:7], -1, 0
	s_cmp_eq_u32 s9, 0
	s_cselect_b32 s9, 0xb3, 0
	s_add_i32 s0, s8, s0
	s_add_i32 s29, s0, s1
	s_add_i32 s29, s29, s9
	v_readlane_b32 s0, v251, 3
	s_cmp_ge_i32 s0, s29
	s_barrier
	s_barrier
	s_cbranch_scc1 .LBB0_2768
	s_and_b64 s[0:1], s[10:11], exec
	v_readlane_b32 s1, v251, 3
	s_cselect_b32 s34, 0x190, 0
	s_cmpk_lt_i32 s1, 0x84
	s_cbranch_scc1 .LBB0_73
	s_andn2_b64 vcc, exec, s[4:5]
	s_cbranch_vccnz .LBB0_54
	v_readlane_b32 s0, v251, 3
	s_add_i32 s13, s0, 0x145
	s_mov_b64 s[0:1], -1
	s_cbranch_execz .LBB0_55
	s_branch .LBB0_56

.LBB0_2822:
	v_readlane_b32 s23, v251, 3
	v_readlane_b32 s10, v251, 2
	s_lshl_b32 s0, s23, 3
	s_lshl_b32 s33, s10, 3
	v_writelane_b32 v251, s0, 61
	s_lshl_b32 s0, s10, 4
	v_writelane_b32 v251, s0, 62
	s_add_u32 s0, s18, 0x200
	s_addc_u32 s1, s19, 0
	v_writelane_b32 v251, s0, 63
	s_waitcnt vmcnt(2)
	v_mov_b32_e32 v3, 0
	v_readlane_b32 s24, v251, 4
	v_writelane_b32 v252, s1, 0
	s_add_u32 s0, s18, 0x1000
	s_addc_u32 s1, s19, 0
	v_writelane_b32 v252, s0, 1
	v_mov_b32_e32 v220, 0x358637bd
	v_mov_b32_e32 v221, 0x260
	v_writelane_b32 v252, s1, 2
	s_add_u32 s0, s18, 0x1100
	s_addc_u32 s1, s19, 0
	v_writelane_b32 v252, s0, 3
	v_mov_b32_e32 v222, 1
	s_mov_b32 s95, 0x20000
	v_writelane_b32 v252, s1, 4
	s_add_u32 s0, s18, 0x1200
	s_addc_u32 s1, s19, 0
	v_writelane_b32 v252, s0, 5
	s_mov_b32 s94, 0x7ffffff0
	v_mov_b32_e32 v247, 0x7f800000
	v_writelane_b32 v252, s1, 6
	s_add_u32 s0, s18, 0x1300
	s_addc_u32 s1, s19, 0
	v_writelane_b32 v252, s0, 7
	s_cmp_eq_u32 s28, 15
	v_mov_b32_e32 v192, 0x3f317218
	v_writelane_b32 v252, s1, 8
	s_cselect_b64 s[0:1], -1, 0
	v_writelane_b32 v252, s0, 9
	s_cmp_eq_u32 s28, 14
	s_mov_b32 s96, 0xf800000
	v_writelane_b32 v252, s1, 10
	s_cselect_b64 s[0:1], -1, 0
	v_writelane_b32 v252, s0, 11
	s_cmp_eq_u32 s28, 13
	s_mov_b64 s[36:37], -1
	v_writelane_b32 v252, s1, 12
	s_cselect_b64 s[0:1], -1, 0
	v_writelane_b32 v252, s0, 13
	s_cmp_eq_u32 s28, 12
	s_mov_b64 s[82:83], 0x80
	v_writelane_b32 v252, s1, 14
	s_cselect_b64 s[0:1], -1, 0
	v_writelane_b32 v252, s0, 15
	s_cmp_eq_u32 s28, 11
	s_nop 0
	v_writelane_b32 v252, s1, 16
	s_cselect_b64 s[0:1], -1, 0
	v_writelane_b32 v252, s0, 17
	s_cmp_eq_u32 s28, 10
	s_nop 0
	v_writelane_b32 v252, s1, 18
	s_cselect_b64 s[0:1], -1, 0
	v_writelane_b32 v252, s0, 19
	s_cmp_eq_u32 s28, 9
	s_nop 0
	v_writelane_b32 v252, s1, 20
	s_cselect_b64 s[0:1], -1, 0
	v_writelane_b32 v252, s0, 21
	s_cmp_eq_u32 s28, 8
	s_nop 0
	v_writelane_b32 v252, s1, 22
	s_cselect_b64 s[0:1], -1, 0
	v_writelane_b32 v252, s0, 23
	s_cmp_eq_u32 s28, 7
	s_nop 0
	v_writelane_b32 v252, s1, 24
	s_cselect_b64 s[0:1], -1, 0
	v_writelane_b32 v252, s0, 25
	s_cmp_eq_u32 s28, 6
	s_nop 0
	v_writelane_b32 v252, s1, 26
	s_cselect_b64 s[0:1], -1, 0
	v_writelane_b32 v252, s0, 27
	s_cmp_eq_u32 s28, 5
	s_nop 0
	v_writelane_b32 v252, s1, 28
	s_cselect_b64 s[0:1], -1, 0
	v_writelane_b32 v252, s0, 29
	s_cmp_eq_u32 s28, 4
	s_nop 0
	v_writelane_b32 v252, s1, 30
	s_cselect_b64 s[0:1], -1, 0
	v_writelane_b32 v252, s0, 31
	s_cmp_eq_u32 s28, 3
	s_nop 0
	v_writelane_b32 v252, s1, 32
	s_cselect_b64 s[0:1], -1, 0
	v_writelane_b32 v252, s0, 33
	s_cmp_eq_u32 s28, 2
	s_nop 0
	v_writelane_b32 v252, s1, 34
	s_cselect_b64 s[0:1], -1, 0
	v_writelane_b32 v252, s0, 35
	s_cmp_eq_u32 s28, 1
	s_nop 0
	v_writelane_b32 v252, s1, 36
	s_cselect_b64 s[0:1], -1, 0
	v_writelane_b32 v252, s0, 37
	s_cmp_eq_u32 s28, 0
	s_nop 0
	v_writelane_b32 v252, s1, 38
	s_cselect_b64 s[0:1], -1, 0
	v_writelane_b32 v252, s0, 39
	s_nop 1
	v_writelane_b32 v252, s1, 40
	s_lshl_b32 s0, s28, 8
	s_add_u32 s0, s18, s0
	s_addc_u32 s1, s19, 0
	s_add_u32 s2, s0, 0x1400
	s_addc_u32 s3, s1, 0
	v_writelane_b32 v252, s2, 41
	s_add_u32 s0, s0, 0x2400
	s_addc_u32 s1, s1, 0
	v_writelane_b32 v252, s3, 42
	v_writelane_b32 v252, s0, 43
	s_nop 1
	v_writelane_b32 v252, s1, 44
	s_add_u32 s0, s18, 0x3400
	s_addc_u32 s1, s19, 0
	v_writelane_b32 v252, s0, 45
	s_nop 1
	v_writelane_b32 v252, s1, 46
	s_add_u32 s0, s18, 0x3500
	s_addc_u32 s1, s19, 0
	s_add_u32 s80, s18, 0x3cc90000
	v_writelane_b32 v252, s0, 47
	s_addc_u32 s81, s19, 0
	s_nop 0
	v_writelane_b32 v252, s1, 48
	s_add_u32 s0, s18, 0x610000
	v_writelane_b32 v252, s0, 49
	s_addc_u32 s0, s19, 0
	v_writelane_b32 v252, s0, 50
	s_add_u32 s0, s18, 0x41490000
	s_addc_u32 s1, s19, 0
	v_writelane_b32 v252, s0, 51
	s_nop 1
	v_writelane_b32 v252, s1, 52
	s_add_u32 s0, s18, 0x4b690000
	s_addc_u32 s1, s19, 0
	v_writelane_b32 v252, s0, 53
	s_nop 1
	v_writelane_b32 v252, s1, 54
	s_and_b32 s1, s23, 7
	s_ashr_i32 s0, s23, 3
	s_cmp_gt_i32 s0, 30
	s_cselect_b64 s[2:3], -1, 0
	s_cmpk_eq_i32 s10, 0x100
	s_cselect_b64 s[12:13], -1, 0
	s_and_b64 s[4:5], s[12:13], exec
	s_cselect_b32 s4, 0x640, 0
	v_writelane_b32 v252, s4, 55
	s_and_b64 s[2:3], s[2:3], s[12:13]
	v_writelane_b32 v252, s2, 56
	s_mul_i32 s6, s1, 31
	s_add_i32 s6, s6, s0
	v_writelane_b32 v252, s3, 57
	s_add_i32 s2, s0, s1
	s_sub_i32 s2, s2, 31
	v_writelane_b32 v252, s2, 58
	s_lshl_b32 s2, s1, 2
	s_sub_i32 s7, s6, s2
	s_cmpk_lg_i32 s10, 0x100
	s_cselect_b32 s2, s10, 0xf8
	s_cselect_b32 s11, s24, s6
	v_writelane_b32 v252, s2, 59
	s_cselect_b32 s2, s10, 0xd8
	s_cselect_b32 s14, s24, s7
	s_cmpk_lt_i32 s11, 0x4c0
	v_writelane_b32 v252, s2, 60
	s_cselect_b64 s[2:3], -1, 0
	v_writelane_b32 v252, s2, 61
	s_and_b32 s6, s11, 7
	s_mul_i32 s20, s1, 5
	v_writelane_b32 v252, s3, 62
	s_add_i32 s2, s11, 0xfffffb80
	s_lshr_b32 s3, s2, 3
	s_cmp_lt_u32 s2, 48
	s_cselect_b32 s4, 8, 10
	s_cmp_gt_u32 s2, 31
	s_cselect_b32 s2, s4, 2
	s_add_i32 s3, s2, s3
	s_mul_hi_i32 s2, s11, 0x38e38e39
	s_lshr_b32 s4, s2, 31
	s_ashr_i32 s2, s2, 5
	s_add_i32 s2, s2, s4
	s_mul_i32 s4, s2, 0x90
	s_sub_i32 s4, s11, s4
	s_mul_i32 s2, s2, 9
	s_and_b32 s5, s4, 7
	s_add_i32 s2, s2, s5
	s_add_i32 s8, s2, 1
	s_ashr_i32 s9, s4, 3
	s_cmp_gt_i32 s0, 26
	s_cselect_b64 s[4:5], -1, 0
	v_writelane_b32 v252, s12, 63
	s_and_b64 s[4:5], s[4:5], s[12:13]
	s_add_i32 s2, s0, s20
	v_writelane_b32 v253, s13, 0
	v_writelane_b32 v253, s4, 1
	s_sub_i32 s2, s2, 27
	s_cmpk_lt_i32 s14, 0x510
	v_writelane_b32 v253, s5, 2
	v_writelane_b32 v253, s2, 3
	s_cselect_b64 s[4:5], -1, 0
	s_mul_hi_i32 s2, s14, 0x38e38e39
	v_writelane_b32 v253, s4, 4
	s_mul_i32 s6, s6, 9
	s_nop 0
	v_writelane_b32 v253, s5, 5
	s_lshr_b32 s4, s2, 31
	s_ashr_i32 s2, s2, 5
	s_add_i32 s2, s2, s4
	s_mul_i32 s4, s2, 0x90
	s_sub_i32 s4, s14, s4
	s_lshl_b32 s2, s2, 3
	s_and_b32 s5, s4, 7
	s_or_b32 s12, s5, s2
	v_writelane_b32 v253, s14, 6
	s_mov_b32 s2, s12
	s_ashr_i32 s14, s4, 3
	v_writelane_b32 v253, s2, 7
	s_ashr_i32 s13, s12, 31
	s_ashr_i32 s15, s14, 31
	v_writelane_b32 v253, s3, 8
	s_mov_b32 s2, s14
	v_writelane_b32 v253, s2, 9
	s_lshl_b64 s[4:5], s[12:13], 20
	s_lshl_b64 s[12:13], s[14:15], 20
	v_writelane_b32 v253, s3, 10
	v_writelane_b32 v253, s12, 11
	s_add_u32 s4, s80, s4
	s_addc_u32 s5, s81, s5
	v_writelane_b32 v253, s13, 12
	s_add_u32 s12, s4, 0x80000
	v_writelane_b32 v253, s4, 13
	s_addc_u32 s13, s5, 0
	s_nop 0
	v_writelane_b32 v253, s5, 14
	v_writelane_b32 v253, s12, 15
	s_nop 1
	v_writelane_b32 v253, s13, 16
	s_add_u32 s12, s18, 0x4ec90000
	s_addc_u32 s13, s19, 0
	s_add_u32 s2, s18, 0x3a10000
	v_writelane_b32 v253, s2, 17
	s_addc_u32 s2, s19, 0
	s_add_u32 s4, s18, 0x50790000
	v_writelane_b32 v253, s2, 18
	s_addc_u32 s5, s19, 0
	v_writelane_b32 v253, s4, 19
	s_cmpk_lt_i32 s24, 0xd8
	s_mul_hi_i32 s2, s24, 0x2aaaaaab
	v_writelane_b32 v253, s5, 20
	s_cselect_b64 s[4:5], -1, 0
	v_writelane_b32 v253, s4, 21
	s_nop 1
	v_writelane_b32 v253, s5, 22
	s_lshr_b32 s4, s2, 31
	s_ashr_i32 s2, s2, 2
	s_add_i32 s2, s2, s4
	s_mul_i32 s4, s2, 24
	s_sub_i32 s4, s24, s4
	s_lshl_b32 s2, s2, 3
	s_and_b32 s5, s4, 7
	s_or_b32 s14, s5, s2
	s_mov_b32 s2, s14
	s_ashr_i32 s16, s4, 3
	v_writelane_b32 v253, s2, 23
	s_ashr_i32 s15, s14, 31
	s_ashr_i32 s17, s16, 31
	v_writelane_b32 v253, s3, 24
	s_mov_b32 s2, s16
	v_writelane_b32 v253, s2, 25
	s_lshl_b64 s[4:5], s[14:15], 18
	s_lshl_b64 s[14:15], s[16:17], 18
	v_writelane_b32 v253, s3, 26
	v_writelane_b32 v253, s14, 27
	s_add_u32 s4, s12, s4
	s_addc_u32 s5, s13, s5
	v_writelane_b32 v253, s15, 28
	v_writelane_b32 v253, s12, 29
	v_writelane_b32 v253, s13, 30
	s_add_u32 s12, s4, 0x20000
	v_writelane_b32 v253, s4, 31
	s_addc_u32 s13, s5, 0
	s_add_u32 s14, s18, 0x4fe90000
	v_writelane_b32 v253, s5, 32
	v_writelane_b32 v253, s12, 33
	s_addc_u32 s15, s19, 0
	s_add_u32 s2, s18, 0x3b90000
	v_writelane_b32 v253, s13, 34
	v_writelane_b32 v253, s2, 35
	s_addc_u32 s2, s19, 0
	s_add_i32 s21, s24, 40
	s_add_u32 s4, s18, 0x52290000
	v_writelane_b32 v253, s2, 36
	s_addc_u32 s5, s19, 0
	v_writelane_b32 v253, s4, 37
	s_cmp_lt_i32 s23, 64
	s_nop 0
	v_writelane_b32 v253, s5, 38
	s_cselect_b64 s[4:5], -1, 0
	v_writelane_b32 v253, s4, 39
	s_and_b32 s2, s23, 1
	s_bfe_u32 s12, s23, 0x20001
	v_writelane_b32 v253, s5, 40
	s_lshl_b32 s4, s2, 3
	s_add_i32 s4, s4, s0
	s_lshl_b32 s4, s4, 2
	s_or_b32 s22, s4, s12
	s_bfe_i32 s13, s23, 0x10000
	s_bitcmp1_b32 s23, 0
	s_cselect_b64 s[4:5], -1, 0
	v_writelane_b32 v253, s4, 41
	s_cmp_eq_u32 s2, 0
	s_mov_b32 s2, 0x57c90000
	v_writelane_b32 v253, s5, 42
	s_cselect_b64 s[4:5], -1, 0
	v_writelane_b32 v253, s4, 43
	s_nop 1
	v_writelane_b32 v253, s5, 44
	s_and_b64 s[4:5], s[4:5], exec
	s_cselect_b32 s2, s2, 0x5a090000
	v_writelane_b32 v253, s2, 45
	s_and_b32 s2, s13, 0xc0
	s_mul_i32 s4, s0, 0x900
	s_or_b32 s23, s2, s4
	s_lshl_b32 s2, s12, 7
	v_writelane_b32 v253, s4, 46
	s_add_u32 s4, s18, 0x5c490000
	v_writelane_b32 v253, s4, 47
	s_addc_u32 s4, s19, 0
	v_writelane_b32 v253, s4, 48
	s_add_u32 s4, s18, 0x2a10000
	v_writelane_b32 v253, s4, 49
	s_addc_u32 s4, s19, 0
	v_writelane_b32 v253, s4, 50
	s_add_u32 s4, s18, 0x33c90000
	s_addc_u32 s5, s19, 0
	v_writelane_b32 v253, s4, 51
	s_cmp_gt_i32 s0, 23
	s_cselect_b64 s[12:13], -1, 0
	v_writelane_b32 v253, s5, 52
	s_mul_i32 s4, s1, -3
	s_add_i32 s5, s7, s4
	v_writelane_b32 v253, s12, 53
	s_cmp_lg_u64 s[76:77], 0
	s_nop 0
	v_writelane_b32 v253, s13, 54
	s_cselect_b64 s[12:13], -1, 0
	s_lshl_b32 s4, s1, 3
	v_writelane_b32 v253, s12, 55
	s_add_i32 s4, s0, s4
	s_sub_i32 s4, s4, 24
	v_writelane_b32 v253, s13, 56
	v_writelane_b32 v253, s4, 57
	s_add_u32 s4, s18, 0x3c90000
	v_writelane_b32 v253, s4, 58
	s_addc_u32 s4, s19, 0
	s_add_u32 s12, s18, 0x4a8000
	v_writelane_b32 v253, s4, 59
	s_addc_u32 s13, s19, 0
	v_writelane_b32 v253, s12, 60
	s_mul_i32 s1, s1, 3
	s_nop 0
	v_writelane_b32 v253, s13, 61
	s_add_u32 s12, s18, 0x4bf90000
	s_addc_u32 s13, s19, 0
	v_writelane_b32 v253, s12, 62
	s_add_i32 s7, s24, s10
	s_nop 0
	v_writelane_b32 v253, s13, 63
	s_add_i32 s12, s7, s10
	s_add_i32 s13, s12, s10
	s_add_i32 s16, s13, s10
	s_add_i32 s17, s16, s10
	s_add_i32 s25, s17, s10
	s_add_i32 s26, s25, s10
	s_add_i32 s27, s26, s10
	s_add_i32 s28, s27, s10
	s_add_u32 s30, s18, 0x3cc90080
	s_addc_u32 s31, s19, 0
	v_writelane_b32 v254, s30, 0
	s_add_u32 s4, s18, 0x23c90000
	s_nop 0
	v_writelane_b32 v254, s31, 1
	v_writelane_b32 v254, s4, 2
	s_addc_u32 s4, s19, 0
	s_add_u32 s30, s18, 0x57c90000
	v_writelane_b32 v254, s4, 3
	s_addc_u32 s31, s19, 0
	v_writelane_b32 v254, s30, 4
	s_add_u32 s18, s18, 0x4cc000
	s_addc_u32 s19, s19, 0
	v_writelane_b32 v254, s31, 5
	v_writelane_b32 v254, s18, 6
	s_cmp_gt_i32 s0, 28
	s_nop 0
	v_writelane_b32 v254, s19, 7
	s_cselect_b64 s[18:19], -1, 0
	v_writelane_b32 v254, s18, 8
	s_add_i32 s1, s0, s1
	s_add_i32 s4, s5, s20
	v_writelane_b32 v254, s19, 9
	v_writelane_b32 v254, s5, 10
	s_sub_i32 s1, s1, 29
	v_writelane_b32 v254, s4, 11
	s_cmpk_lt_i32 s11, 0x480
	v_writelane_b32 v254, s1, 12
	s_cselect_b32 s8, s8, s6
	v_writelane_b32 v254, s11, 13
	s_mov_b32 s4, s8
	s_cselect_b32 s18, s9, s3
	v_writelane_b32 v254, s4, 14
	s_ashr_i32 s9, s8, 31
	s_ashr_i32 s19, s18, 31
	v_writelane_b32 v254, s5, 15
	s_mov_b32 s6, s18
	s_lshl_b64 s[4:5], s[8:9], 20
	v_writelane_b32 v254, s6, 16
	s_lshl_b64 s[8:9], s[18:19], 20
	s_add_u32 s4, s80, s4
	v_writelane_b32 v254, s7, 17
	v_writelane_b32 v254, s8, 18
	s_addc_u32 s5, s81, s5
	s_nop 0
	v_writelane_b32 v254, s9, 19
	s_add_u32 s8, s4, 0x80000
	v_writelane_b32 v254, s4, 20
	s_addc_u32 s9, s5, 0
	s_abs_i32 s1, s10
	v_cvt_f32_u32_e32 v1, s1
	v_writelane_b32 v254, s5, 21
	s_sub_i32 s3, 0, s1
	v_writelane_b32 v254, s8, 22
	v_rcp_iflag_f32_e32 v1, v1
	s_lshl_b32 s0, s0, 6
	v_writelane_b32 v254, s9, 23
	s_addk_i32 s0, 0x800
	v_mul_f32_e32 v1, 0x4f7ffffe, v1
	v_cvt_u32_f32_e32 v1, v1
	v_writelane_b32 v254, s0, 24
	s_ashr_i32 s0, s21, 31
	v_readfirstlane_b32 s4, v1
	s_mul_i32 s3, s3, s4
	s_mul_hi_u32 s3, s4, s3
	s_add_i32 s4, s4, s3
	s_abs_i32 s3, s21
	s_mul_hi_u32 s4, s3, s4
	s_mul_i32 s4, s4, s1
	s_sub_i32 s3, s3, s4
	s_sub_i32 s4, s3, s1
	s_cmp_ge_u32 s3, s1
	s_cselect_b32 s3, s4, s3
	s_sub_i32 s4, s3, s1
	s_cmp_ge_u32 s3, s1
	s_cselect_b32 s1, s4, s3
	s_xor_b32 s1, s1, s0
	s_sub_i32 s3, s1, s0
	s_cmpk_lt_i32 s3, 0x120
	s_cselect_b64 s[0:1], -1, 0
	v_writelane_b32 v254, s0, 25
	v_mbcnt_lo_u32_b32 v1, -1, 0
	s_nop 0
	v_writelane_b32 v254, s1, 26
	s_ashr_i32 s0, s3, 31
	s_lshr_b32 s0, s0, 27
	s_add_i32 s0, s3, s0
	s_ashr_i32 s1, s0, 5
	s_andn2_b32 s0, s0, 31
	s_sub_i32 s0, s3, s0
	v_writelane_b32 v254, s3, 27
	s_lshl_b32 s1, s1, 3
	s_and_b32 s3, s0, 7
	s_or_b32 s4, s3, s1
	s_ashr_i32 s8, s0, 3
	s_mov_b32 s0, s4
	s_ashr_i32 s5, s4, 31
	v_writelane_b32 v254, s0, 28
	s_ashr_i32 s9, s8, 31
	s_mul_hi_i32 s3, s23, 0x2400
	v_writelane_b32 v254, s1, 29
	s_lshl_b64 s[0:1], s[4:5], 17
	s_mov_b32 s4, s8
	v_writelane_b32 v254, s4, 30
	v_mbcnt_hi_u32_b32 v224, -1, v1
	s_nop 0
	v_writelane_b32 v254, s5, 31
	s_lshl_b64 s[4:5], s[8:9], 17
	v_writelane_b32 v254, s4, 32
	s_nop 1
	v_writelane_b32 v254, s5, 33
	v_writelane_b32 v254, s14, 34
	v_writelane_b32 v254, s15, 35
	s_add_u32 s4, s14, s0
	v_writelane_b32 v254, s3, 36
	s_mul_i32 s3, s23, 0x2400
	s_addc_u32 s5, s15, s1
	v_writelane_b32 v254, s3, 37
	s_add_u32 s8, s4, 0x10000
	v_writelane_b32 v254, s4, 38
	s_addc_u32 s9, s5, 0
	s_mul_hi_i32 s1, s22, 0x900
	v_writelane_b32 v254, s5, 39
	s_mul_i32 s0, s22, 0x900
	v_writelane_b32 v254, s8, 40
	s_lshl_b64 s[0:1], s[0:1], 2
	s_nop 0
	v_writelane_b32 v254, s9, 41
	v_writelane_b32 v254, s0, 42
	s_nop 1
	v_writelane_b32 v254, s1, 43
	s_lshl_b32 s0, s2, 1
	v_writelane_b32 v254, s0, 44
	s_ashr_i32 s0, s24, 31
	v_writelane_b32 v254, s0, 45
	s_abs_i32 s0, s24
	v_writelane_b32 v254, s0, 46
	s_ashr_i32 s0, s7, 31
	v_writelane_b32 v254, s0, 47
	v_writelane_b32 v254, s7, 48
	s_abs_i32 s0, s7
	v_writelane_b32 v254, s0, 49
	s_ashr_i32 s0, s12, 31
	v_writelane_b32 v254, s0, 50
	v_writelane_b32 v254, s12, 51
	s_abs_i32 s0, s12
	v_writelane_b32 v254, s0, 52
	s_ashr_i32 s0, s13, 31
	v_writelane_b32 v254, s0, 53
	v_writelane_b32 v254, s13, 54
	s_abs_i32 s0, s13
	v_writelane_b32 v254, s0, 55
	s_ashr_i32 s0, s16, 31
	v_writelane_b32 v254, s0, 56
	v_writelane_b32 v254, s16, 57
	s_abs_i32 s0, s16
	v_writelane_b32 v254, s0, 58
	s_ashr_i32 s0, s17, 31
	v_writelane_b32 v254, s0, 59
	v_writelane_b32 v254, s17, 60
	s_abs_i32 s0, s17
	v_writelane_b32 v254, s0, 61
	s_ashr_i32 s0, s25, 31
	v_writelane_b32 v254, s0, 62
	s_abs_i32 s0, s25
	v_writelane_b32 v255, s0, 0
	s_ashr_i32 s0, s26, 31
	v_writelane_b32 v255, s0, 1
	v_writelane_b32 v255, s26, 2
	s_abs_i32 s0, s26
	v_writelane_b32 v255, s0, 3
	s_ashr_i32 s0, s27, 31
	v_writelane_b32 v255, s0, 4
	v_writelane_b32 v255, s27, 5
	s_abs_i32 s0, s27
	v_writelane_b32 v255, s0, 6
	s_ashr_i32 s0, s28, 31
	v_writelane_b32 v255, s0, 7
	v_writelane_b32 v255, s28, 8
	s_abs_i32 s0, s28
	v_writelane_b32 v255, s0, 9
	s_mul_i32 s0, s10, 24
	v_writelane_b32 v255, s0, 10
	s_add_i32 s0, 0, 0x25fc0
	v_writelane_b32 v255, s0, 11
	s_add_i32 s0, 0, 0x25fc4
	v_writelane_b32 v255, s0, 12
	s_add_i32 s0, 0, 0x1e800
	v_writelane_b32 v255, s0, 13
	s_add_i32 s0, 0, 0x21700
	v_writelane_b32 v255, s0, 14
	s_add_i32 s0, 0, 0x21600
	v_writelane_b32 v255, s0, 15
	s_add_i32 s0, 0, 0x20e00
	v_writelane_b32 v255, s0, 16
	s_add_i32 s0, 0, 0x11c00
	v_writelane_b32 v255, s0, 17
	s_add_i32 s0, 0, 0x25fd0
	v_writelane_b32 v255, s0, 18
	s_add_i32 s0, 0, 0x20200
	s_mov_b32 s7, 0
	v_writelane_b32 v254, s25, 63
	v_writelane_b32 v255, s0, 19
	s_mov_b32 s2, s7
	s_branch .LBB0_2826

.LBB0_6849:
	v_max_f32_e32 v2, v201, v201
	v_max_f32_e32 v1, v1, v1
	v_max_f32_e32 v1, v1, v2
	v_max_f32_e32 v2, v200, v200
	s_nop 1
	v_max_f32_e32 v4, v199, v199
	v_mul_f32_e32 v1, 0x418293ee, v1
	v_max_f32_e32 v2, v4, v2
	v_mul_f32_e32 v1, v2, v1
	s_mov_b32 s2, 0x42c00000
	v_cmp_ngt_f32_e32 vcc, s2, v1
	s_ashr_i32 s50, s62, 6
	v_lshlrev_b32_e32 v2, 4, v197
	v_cndmask_b32_e64 v1, 0, 1, vcc
	s_waitcnt vmcnt(4)
	v_ashrrev_i32_e32 v168, 3, v197
	v_readfirstlane_b32 s2, v1
	s_bitcmp1_b32 s2, 0
	s_cselect_b64 s[2:3], -1, 0
	s_xor_b64 s[44:45], s[2:3], -1
	s_add_u32 s0, s60, s0
	s_addc_u32 s1, s61, s1
	s_add_u32 s46, s0, 0x4100
	s_addc_u32 s47, s1, 0
	s_and_b64 s[0:1], s[36:37], exec
	s_movk_i32 s0, 0x240
	s_cselect_b32 s51, s0, 0x200
	s_movk_i32 s0, 0x4f4
	s_cselect_b32 s52, s0, 0xb46
	s_add_i32 s53, s51, 0x48
	v_readlane_b32 s0, v252, 55
	s_add_i32 s54, s53, s0
	s_and_b64 s[0:1], s[36:37], exec
	s_movk_i32 s0, 0xfd78
	s_cselect_b32 s55, s0, 0xfffffdb8
	s_add_u32 s9, s60, 0x23c90000
	s_addc_u32 s57, s61, 0
	s_add_u32 s58, s60, 0x3c90000
	s_addc_u32 s59, s61, 0
	s_add_u32 s62, s60, 0x3b90000
	s_addc_u32 s63, s61, 0
	s_add_u32 s85, s60, 0x3a10000
	s_addc_u32 s86, s61, 0
	v_lshlrev_b32_e32 v1, 2, v197
	s_add_u32 s87, s60, 0x2a10000
	v_and_b32_e32 v4, 0x70, v2
	s_movk_i32 s0, 0x108
	v_ashrrev_i32_e32 v2, 1, v197
	v_and_b32_e32 v171, 60, v1
	s_addc_u32 s88, s61, 0
	v_and_b32_e32 v8, -8, v2
	v_mul_lo_u32 v2, v168, s0
	s_add_u32 s89, s60, 0x610000
	v_mad_u32_u24 v5, v171, s0, 0
	v_add_u32_e32 v9, 0, v2
	v_lshlrev_b32_e32 v2, 5, v197
	v_readlane_b32 s0, v255, 20
	s_addc_u32 s90, s61, 0
	v_and_b32_e32 v10, 0xe0, v2
	v_readlane_b32 s1, v255, 21
	s_mov_b32 s2, s0
	s_lshl_b32 s0, s0, 3
	v_lshlrev_b32_e32 v2, 4, v198
	s_or_b32 s84, s0, 32
	v_lshl_add_u64 v[6:7], s[60:61], 0, v[2:3]
	s_mov_b64 s[0:1], 0x57c90000
	s_waitcnt vmcnt(3)
	v_lshl_add_u64 v[174:175], v[6:7], 0, s[0:1]
	s_mov_b64 s[0:1], 0x5a090000
	s_lshl_b32 s6, s2, 9
	s_waitcnt vmcnt(2)
	v_lshl_add_u64 v[176:177], v[6:7], 0, s[0:1]
	s_add_u32 s0, s60, 0x5c490000
	s_addc_u32 s1, s61, 0
	s_add_u32 s91, s60, 0x4e390000
	s_addc_u32 s8, s61, 0
	s_add_u32 s97, s60, 0x4bf90000
	v_readlane_b32 s64, v251, 5
	v_lshl_add_u64 v[178:179], s[0:1], 0, v[2:3]
	s_addc_u32 s56, s61, 0
	s_lshl_b64 s[0:1], s[6:7], 2
	v_readlane_b32 s68, v251, 9
	v_ashrrev_i32_e32 v1, 2, v197
	v_readlane_b32 s69, v251, 10
	s_add_u32 s0, s68, s0
	v_and_b32_e32 v170, -4, v1
	s_addc_u32 s1, s69, s1
	v_lshlrev_b32_e32 v2, 5, v198
	v_ashrrev_i32_e32 v1, 31, v170
	v_ashrrev_i32_e32 v169, 31, v168
	v_lshlrev_b32_e32 v172, 3, v198
	s_waitcnt vmcnt(1)
	v_lshl_add_u64 v[180:181], s[0:1], 0, v[2:3]
	v_lshlrev_b32_e32 v182, 1, v4
	v_add_u32_e32 v173, v5, v8
	s_waitcnt vmcnt(0)
	v_add_u32_e32 v184, v9, v10
	v_readlane_b32 s65, v251, 6
	v_readlane_b32 s66, v251, 7
	v_readlane_b32 s67, v251, 8
	v_readlane_b32 s70, v251, 11
	v_readlane_b32 s71, v251, 12
	v_readlane_b32 s72, v251, 13
	v_readlane_b32 s73, v251, 14
	v_readlane_b32 s74, v251, 15
	v_readlane_b32 s75, v251, 16
	v_readlane_b32 s76, v251, 17
	v_readlane_b32 s77, v251, 18
	v_readlane_b32 s78, v251, 19
	v_readlane_b32 s79, v251, 20
	s_branch .LBB0_6853
